# global attention loop: fewer VALU (running KV pointers, deferred cross-half l combine), counted PV waits
# speedup vs baseline: 1.0343x; 1.0158x over previous
.LBB0_591:
	global_load_dwordx4 v[140:143], v[150:151], off
	global_load_dwordx4 v[136:139], v[150:151], off offset:32
	global_load_dwordx4 v[132:135], v[150:151], off offset:64
	global_load_dwordx4 v[128:131], v[150:151], off offset:96
	global_load_dwordx4 v[124:127], v[150:151], off offset:128
	global_load_dwordx4 v[120:123], v[150:151], off offset:160
	global_load_dwordx4 v[116:119], v[150:151], off offset:192
	global_load_dwordx4 v[112:115], v[150:151], off offset:224
	global_load_dwordx4 v[0:3], v[152:153], off
	global_load_dwordx4 v[4:7], v[154:155], off
	global_load_dwordx4 v[8:11], v[156:157], off
	global_load_dwordx4 v[12:15], v[158:159], off
	s_waitcnt vmcnt(0)
	s_add_u32 s10, s6, 0x90000
	s_addc_u32 s11, s7, 0
	s_add_u32 s22, s8, 0x90000
	s_addc_u32 s23, s9, 0
	s_add_u32 s6, s6, 0x120000
	s_addc_u32 s7, s7, 0
	s_add_u32 s8, s8, 0x120000
	s_addc_u32 s9, s9, 0
	s_cmp_lg_u32 0, -1
	v_mov_b32_e32 v183, 0
	v_mov_b32_e32 v194, 0x8000
	v_mov_b32_e32 v216, 0xc000
	v_mov_b32_e32 v187, v193
	v_mov_b32_e32 v24, v183
	v_mov_b32_e32 v25, v183
	v_mov_b32_e32 v26, v183
	v_mov_b32_e32 v27, v183
	v_mov_b32_e32 v28, v183
	v_mov_b32_e32 v29, v183
	v_mov_b32_e32 v30, v183
	v_mov_b32_e32 v31, v183
	v_mov_b32_e32 v32, 0
	v_mov_b32_e32 v33, v183
	v_mov_b32_e32 v34, v183
	v_mov_b32_e32 v35, v183
	v_mov_b32_e32 v36, v183
	v_mov_b32_e32 v37, v183
	v_mov_b32_e32 v38, v183
	v_mov_b32_e32 v39, v183
	v_mov_b32_e32 v40, v183
	v_mov_b32_e32 v41, v183
	v_mov_b32_e32 v42, v183
	v_mov_b32_e32 v43, v183
	v_mov_b32_e32 v44, v183
	v_mov_b32_e32 v45, v183
	v_mov_b32_e32 v46, v183
	v_mov_b32_e32 v47, v183
	v_mov_b32_e32 v48, 0
	v_mov_b32_e32 v49, v183
	v_mov_b32_e32 v50, v183
	v_mov_b32_e32 v51, v183
	v_mov_b32_e32 v52, v183
	v_mov_b32_e32 v53, v183
	v_mov_b32_e32 v54, v183
	v_mov_b32_e32 v55, v183
	v_mov_b32_e32 v56, v183
	v_mov_b32_e32 v57, v183
	v_mov_b32_e32 v58, v183
	v_mov_b32_e32 v59, v183
	v_mov_b32_e32 v60, v183
	v_mov_b32_e32 v61, v183
	v_mov_b32_e32 v62, v183
	v_mov_b32_e32 v63, v183
	s_waitcnt vmcnt(3)
	ds_write_b128 v204, v[0:3]
	s_waitcnt vmcnt(2)
	ds_write_b128 v205, v[4:7]
	s_waitcnt vmcnt(1)
	ds_write_b128 v206, v[8:11] offset:32768
	s_waitcnt vmcnt(0)
	ds_write_b128 v207, v[12:15] offset:32768
	v_bitop3_b32 v0, v184, v175, v188 bitop3:0xde
	v_add_u32_e32 v212, 0, v0
	s_waitcnt lgkmcnt(0)
	s_barrier
	ds_read_b128 v[0:3], v212 offset:32768
	ds_read_b128 v[16:19], v212 offset:40960
	s_waitcnt lgkmcnt(1)
	v_mfma_f32_32x32x16_bf16 v[0:15], v[0:3], v[140:143], 0
	s_waitcnt lgkmcnt(0)
	v_mfma_f32_32x32x16_bf16 v[64:79], v[16:19], v[140:143], 0
	v_bitop3_b32 v16, v211, v175, v188 bitop3:0xde
	v_add_u32_e32 v211, 0, v16
	ds_read_b128 v[16:19], v211 offset:32768
	ds_read_b128 v[20:23], v211 offset:40960
	s_waitcnt lgkmcnt(1)
	v_mfma_f32_32x32x16_bf16 v[0:15], v[16:19], v[136:139], v[0:15]
	v_bitop3_b32 v16, v210, v175, v188 bitop3:0xde
	v_add_u32_e32 v210, 0, v16
	s_waitcnt lgkmcnt(0)
	v_mfma_f32_32x32x16_bf16 v[64:79], v[20:23], v[136:139], v[64:79]
	ds_read_b128 v[16:19], v210 offset:32768
	ds_read_b128 v[20:23], v210 offset:40960
	s_waitcnt lgkmcnt(1)
	v_mfma_f32_32x32x16_bf16 v[0:15], v[16:19], v[132:135], v[0:15]
	v_bitop3_b32 v16, v209, v175, v188 bitop3:0xde
	v_add_u32_e32 v209, 0, v16
	s_waitcnt lgkmcnt(0)
	v_mfma_f32_32x32x16_bf16 v[64:79], v[20:23], v[132:135], v[64:79]
	ds_read_b128 v[16:19], v209 offset:32768
	ds_read_b128 v[20:23], v209 offset:40960
	s_waitcnt lgkmcnt(1)
	v_mfma_f32_32x32x16_bf16 v[0:15], v[16:19], v[128:131], v[0:15]
	v_bitop3_b32 v16, v208, v175, v188 bitop3:0xde
	v_add_u32_e32 v208, 0, v16
	s_waitcnt lgkmcnt(0)
	v_mfma_f32_32x32x16_bf16 v[64:79], v[20:23], v[128:131], v[64:79]
	ds_read_b128 v[16:19], v208 offset:32768
	ds_read_b128 v[20:23], v208 offset:40960
	s_waitcnt lgkmcnt(1)
	v_mfma_f32_32x32x16_bf16 v[0:15], v[16:19], v[124:127], v[0:15]
	v_bitop3_b32 v16, v191, v175, v188 bitop3:0xde
	v_add_u32_e32 v213, 0, v16
	s_waitcnt lgkmcnt(0)
	v_mfma_f32_32x32x16_bf16 v[64:79], v[20:23], v[124:127], v[64:79]
	ds_read_b128 v[16:19], v213 offset:32768
	ds_read_b128 v[20:23], v213 offset:40960
	s_waitcnt lgkmcnt(1)
	v_mfma_f32_32x32x16_bf16 v[0:15], v[16:19], v[120:123], v[0:15]
	v_bitop3_b32 v16, v190, v175, v188 bitop3:0xde
	v_add_u32_e32 v214, 0, v16
	s_waitcnt lgkmcnt(0)
	v_mfma_f32_32x32x16_bf16 v[64:79], v[20:23], v[120:123], v[64:79]
	ds_read_b128 v[16:19], v214 offset:32768
	ds_read_b128 v[20:23], v214 offset:40960
	s_waitcnt lgkmcnt(1)
	v_mfma_f32_32x32x16_bf16 v[0:15], v[16:19], v[116:119], v[0:15]
	v_bitop3_b32 v16, v189, v175, v188 bitop3:0xde
	v_add_u32_e32 v215, 0, v16
	s_waitcnt lgkmcnt(0)
	v_mfma_f32_32x32x16_bf16 v[64:79], v[20:23], v[116:119], v[64:79]
	ds_read_b128 v[16:19], v215 offset:32768
	ds_read_b128 v[20:23], v215 offset:40960
	s_waitcnt lgkmcnt(1)
	v_mfma_f32_32x32x16_bf16 v[0:15], v[16:19], v[112:115], v[0:15]
	v_lshl_add_u64 v[16:17], s[8:9], 0, v[192:193]
	v_lshl_add_u64 v[18:19], s[8:9], 0, v[148:149]
	s_mov_b32 s8, 1
	s_waitcnt lgkmcnt(0)
	v_mfma_f32_32x32x16_bf16 v[64:79], v[20:23], v[112:115], v[64:79]
	s_nop 6
	v_exp_f32_e32 v231, v0
	v_exp_f32_e32 v233, v1
	v_exp_f32_e32 v228, v4
	v_exp_f32_e32 v230, v5
	v_exp_f32_e32 v223, v8
	v_exp_f32_e32 v225, v9
	v_exp_f32_e32 v188, v12
	v_exp_f32_e32 v191, v13
	v_lshl_add_u64 v[0:1], s[22:23], 0, v[192:193]
	v_lshl_add_u64 v[4:5], s[22:23], 0, v[148:149]
	v_lshl_add_u64 v[8:9], s[10:11], 0, v[192:193]
	v_lshl_add_u64 v[12:13], s[10:11], 0, v[148:149]
	v_exp_f32_e32 v229, v2
	v_exp_f32_e32 v232, v3
	v_exp_f32_e32 v226, v6
	v_exp_f32_e32 v227, v7
	v_exp_f32_e32 v222, v10
	v_exp_f32_e32 v224, v11
	v_exp_f32_e32 v189, v14
	v_exp_f32_e32 v190, v15
	global_load_dwordx4 v[0:3], v[0:1], off
	v_lshl_add_u64 v[20:21], s[6:7], 0, v[192:193]
	global_load_dwordx4 v[4:7], v[4:5], off
	v_lshl_add_u64 v[22:23], s[6:7], 0, v[148:149]
	global_load_dwordx4 v[8:11], v[8:9], off
	s_cselect_b32 s6, 0, 0
	global_load_dwordx4 v[12:15], v[12:13], off
	s_nop 0
	global_load_dwordx4 v[144:147], v[16:17], off
	global_load_dwordx4 v[152:155], v[18:19], off
	global_load_dwordx4 v[148:151], v[20:21], off
	global_load_dwordx4 v[156:159], v[22:23], off
	s_addk_i32 s6, 0x4000
	s_waitcnt vmcnt(4)
	v_add_u32_e32 v177, s6, v174
	v_readlane_b32 s6, v254, 39
	s_add_u32 s2, s6, s2
	v_readlane_b32 s6, v254, 40
	s_waitcnt vmcnt(7)
	ds_write_b128 v204, v[0:3] offset:16384
	s_waitcnt vmcnt(6)
	ds_write_b128 v205, v[4:7] offset:16384
	s_waitcnt vmcnt(5)
	ds_write_b128 v206, v[8:11] offset:49152
	s_waitcnt vmcnt(4)
	ds_write_b128 v207, v[12:15] offset:49152
	s_addc_u32 s3, s6, s3
	v_add_u32_e32 v192, 0x48000, v186
	v_mov_b32_e32 v0, 0
	v_mov_b32_e32 v1, v183
	v_mov_b32_e32 v2, v183
	v_mov_b32_e32 v3, v183
	v_mov_b32_e32 v4, v183
	v_mov_b32_e32 v5, v183
	v_mov_b32_e32 v6, v183
	v_mov_b32_e32 v7, v183
	v_mov_b32_e32 v8, v183
	v_mov_b32_e32 v9, v183
	v_mov_b32_e32 v10, v183
	v_mov_b32_e32 v11, v183
	v_mov_b32_e32 v12, v183
	v_mov_b32_e32 v13, v183
	v_mov_b32_e32 v14, v183
	v_mov_b32_e32 v15, v183
	v_mov_b32_e32 v16, 0
	v_mov_b32_e32 v17, v183
	v_mov_b32_e32 v18, v183
	v_mov_b32_e32 v19, v183
	v_mov_b32_e32 v20, v183
	v_mov_b32_e32 v21, v183
	v_mov_b32_e32 v22, v183
	v_mov_b32_e32 v23, v183
	s_waitcnt lgkmcnt(0)
	s_barrier
	v_lshl_add_u64 v[196:197], s[2:3], 0, v[186:187]
	v_lshl_add_u64 v[198:199], s[2:3], 0, v[192:193]
	s_mov_b64 s[100:101], 0x11921000
	v_lshl_add_u64 v[196:197], v[196:197], 0, s[100:101]
	v_lshl_add_u64 v[198:199], v[198:199], 0, s[100:101]
	s_mov_b64 s[100:101], 0x90000
	s_branch .LBB0_593
.LBB0_592:
	v_add_f32_e32 v183, v183, v234
	v_add_f32_e32 v183, v183, v222
	s_add_i32 s8, s8, 2
	ds_read_b64_tr_b16 v[188:189], v177 offset:0
	ds_read_b64_tr_b16 v[190:191], v177 offset:0x800
	ds_read_b64_tr_b16 v[222:223], v177 offset:0x1000
	ds_read_b64_tr_b16 v[224:225], v177 offset:0x1800
	ds_read_b64_tr_b16 v[226:227], v177 offset:0x2000
	ds_read_b64_tr_b16 v[228:229], v177 offset:0x2800
	ds_read_b64_tr_b16 v[230:231], v177 offset:0x3000
	ds_read_b64_tr_b16 v[232:233], v177 offset:0x3800
	s_waitcnt lgkmcnt(6)
	s_nop 0
	v_mfma_f32_32x32x16_bf16 v[0:15], v[80:83], v[188:191], v[0:15]
	ds_read_b64_tr_b16 v[188:189], v177 offset:0x200
	ds_read_b64_tr_b16 v[190:191], v177 offset:0xa00
	s_waitcnt lgkmcnt(6)
	v_mfma_f32_32x32x16_bf16 v[0:15], v[84:87], v[222:225], v[0:15]
	ds_read_b64_tr_b16 v[222:223], v177 offset:0x1200
	ds_read_b64_tr_b16 v[224:225], v177 offset:0x1a00
	s_waitcnt lgkmcnt(6)
	v_mfma_f32_32x32x16_bf16 v[0:15], v[88:91], v[226:229], v[0:15]
	ds_read_b64_tr_b16 v[226:227], v177 offset:0x2200
	ds_read_b64_tr_b16 v[228:229], v177 offset:0x2a00
	s_waitcnt lgkmcnt(6)
	v_mfma_f32_32x32x16_bf16 v[0:15], v[92:95], v[230:233], v[0:15]
	ds_read_b64_tr_b16 v[230:231], v177 offset:0x3200
	ds_read_b64_tr_b16 v[232:233], v177 offset:0x3a00
	s_waitcnt lgkmcnt(6)
	v_mfma_f32_32x32x16_bf16 v[16:31], v[80:83], v[188:191], v[16:31]
	ds_read_b64_tr_b16 v[188:189], v177 offset:0x400
	ds_read_b64_tr_b16 v[190:191], v177 offset:0xc00
	s_waitcnt lgkmcnt(6)
	v_mfma_f32_32x32x16_bf16 v[16:31], v[84:87], v[222:225], v[16:31]
	ds_read_b64_tr_b16 v[222:223], v177 offset:0x1400
	ds_read_b64_tr_b16 v[224:225], v177 offset:0x1c00
	s_waitcnt lgkmcnt(6)
	v_mfma_f32_32x32x16_bf16 v[16:31], v[88:91], v[226:229], v[16:31]
	ds_read_b64_tr_b16 v[226:227], v177 offset:0x2400
	ds_read_b64_tr_b16 v[228:229], v177 offset:0x2c00
	s_waitcnt lgkmcnt(6)
	v_mfma_f32_32x32x16_bf16 v[16:31], v[92:95], v[230:233], v[16:31]
	ds_read_b64_tr_b16 v[230:231], v177 offset:0x3400
	ds_read_b64_tr_b16 v[232:233], v177 offset:0x3c00
	s_waitcnt lgkmcnt(6)
	v_mfma_f32_32x32x16_bf16 v[32:47], v[80:83], v[188:191], v[32:47]
	ds_read_b64_tr_b16 v[188:189], v177 offset:0x600
	ds_read_b64_tr_b16 v[190:191], v177 offset:0xe00
	s_waitcnt vmcnt(4)
	ds_write_b128 v206, v[164:167] offset:49152
	ds_write_b128 v207, v[168:171] offset:49152
	s_waitcnt lgkmcnt(8)
	v_mfma_f32_32x32x16_bf16 v[32:47], v[84:87], v[222:225], v[32:47]
	ds_read_b64_tr_b16 v[222:223], v177 offset:0x1600
	ds_read_b64_tr_b16 v[224:225], v177 offset:0x1e00
	s_waitcnt lgkmcnt(8)
	v_mfma_f32_32x32x16_bf16 v[32:47], v[88:91], v[226:229], v[32:47]
	ds_read_b64_tr_b16 v[226:227], v177 offset:0x2600
	ds_read_b64_tr_b16 v[228:229], v177 offset:0x2e00
	s_waitcnt lgkmcnt(8)
	v_mfma_f32_32x32x16_bf16 v[32:47], v[92:95], v[230:233], v[32:47]
	ds_read_b64_tr_b16 v[230:231], v177 offset:0x3600
	ds_read_b64_tr_b16 v[232:233], v177 offset:0x3e00
	s_waitcnt lgkmcnt(8)
	v_mfma_f32_32x32x16_bf16 v[48:63], v[80:83], v[188:191], v[48:63]
	v_exp_f32_e32 v188, v108
	v_exp_f32_e32 v191, v109
	v_exp_f32_e32 v189, v110
	v_exp_f32_e32 v190, v111
	s_waitcnt lgkmcnt(0)
	s_barrier
	v_mfma_f32_32x32x16_bf16 v[48:63], v[84:87], v[222:225], v[48:63]
	v_exp_f32_e32 v223, v104
	v_exp_f32_e32 v225, v105
	v_exp_f32_e32 v222, v106
	v_exp_f32_e32 v224, v107
	s_waitcnt vmcnt(4)
	v_mfma_f32_32x32x16_bf16 v[48:63], v[88:91], v[226:229], v[48:63]
	v_exp_f32_e32 v229, v98
	v_exp_f32_e32 v228, v100
	v_exp_f32_e32 v226, v102
	v_exp_f32_e32 v227, v103
	s_and_b64 vcc, exec, s[6:7]
	ds_write_b128 v204, v[160:163] offset:16384
	ds_write_b128 v205, v[172:175] offset:16384
	v_mfma_f32_32x32x16_bf16 v[48:63], v[92:95], v[230:233], v[48:63]
	v_exp_f32_e32 v231, v96
	v_exp_f32_e32 v233, v97
	v_exp_f32_e32 v232, v99
	v_exp_f32_e32 v230, v101
	s_cbranch_vccnz .Lga_exit
.LBB0_593:
	ds_read_b128 v[80:83], v212 offset:49152
	ds_read_b128 v[84:87], v212 offset:57344
	ds_read_b128 v[160:163], v211 offset:49152
	ds_read_b128 v[164:167], v211 offset:57344
	v_exp_f32_e32 v168, v72
	v_exp_f32_e32 v169, v73
	s_waitcnt lgkmcnt(3)
	v_mfma_f32_32x32x16_bf16 v[96:111], v[80:83], v[140:143], 0
	v_exp_f32_e32 v170, v74
	v_exp_f32_e32 v171, v75
	v_exp_f32_e32 v172, v76
	v_exp_f32_e32 v173, v77
	v_exp_f32_e32 v174, v78
	v_exp_f32_e32 v79, v79
	s_waitcnt lgkmcnt(2)
	v_mfma_f32_32x32x16_bf16 v[80:95], v[84:87], v[140:143], 0
	s_waitcnt lgkmcnt(1)
	v_mfma_f32_32x32x16_bf16 v[96:111], v[160:163], v[136:139], v[96:111]
	s_waitcnt lgkmcnt(0)
	v_mfma_f32_32x32x16_bf16 v[80:95], v[164:167], v[136:139], v[80:95]
	ds_read_b128 v[160:163], v210 offset:49152
	ds_read_b128 v[164:167], v210 offset:57344
	s_waitcnt lgkmcnt(1)
	v_mfma_f32_32x32x16_bf16 v[96:111], v[160:163], v[132:135], v[96:111]
	s_waitcnt lgkmcnt(0)
	v_mfma_f32_32x32x16_bf16 v[80:95], v[164:167], v[132:135], v[80:95]
	ds_read_b128 v[160:163], v209 offset:49152
	ds_read_b128 v[164:167], v209 offset:57344
	s_waitcnt lgkmcnt(1)
	v_mfma_f32_32x32x16_bf16 v[96:111], v[160:163], v[128:131], v[96:111]
	s_waitcnt lgkmcnt(0)
	v_mfma_f32_32x32x16_bf16 v[80:95], v[164:167], v[128:131], v[80:95]
	ds_read_b128 v[160:163], v208 offset:49152
	ds_read_b128 v[164:167], v208 offset:57344
	s_waitcnt lgkmcnt(1)
	v_mfma_f32_32x32x16_bf16 v[96:111], v[160:163], v[124:127], v[96:111]
	s_waitcnt lgkmcnt(0)
	v_mfma_f32_32x32x16_bf16 v[80:95], v[164:167], v[124:127], v[80:95]
	ds_read_b128 v[160:163], v213 offset:49152
	ds_read_b128 v[164:167], v213 offset:57344
	s_waitcnt lgkmcnt(1)
	v_mfma_f32_32x32x16_bf16 v[96:111], v[160:163], v[120:123], v[96:111]
	s_waitcnt lgkmcnt(0)
	v_mfma_f32_32x32x16_bf16 v[80:95], v[164:167], v[120:123], v[80:95]
	ds_read_b128 v[160:163], v214 offset:49152
	ds_read_b128 v[164:167], v214 offset:57344
	s_waitcnt lgkmcnt(1)
	v_mfma_f32_32x32x16_bf16 v[96:111], v[160:163], v[116:119], v[96:111]
	s_waitcnt lgkmcnt(0)
	v_mfma_f32_32x32x16_bf16 v[80:95], v[164:167], v[116:119], v[80:95]
	ds_read_b128 v[160:163], v215 offset:49152
	ds_read_b128 v[164:167], v215 offset:57344
	s_waitcnt lgkmcnt(1)
	v_mfma_f32_32x32x16_bf16 v[96:111], v[160:163], v[112:115], v[96:111]
	v_exp_f32_e32 v160, v64
	v_add_f32_e32 v64, v233, v231
	v_add_f32_e32 v64, v229, v64
	v_add_f32_e32 v64, v232, v64
	v_add_f32_e32 v64, v228, v64
	v_add_f32_e32 v64, v230, v64
	v_add_f32_e32 v64, v226, v64
	v_add_f32_e32 v64, v227, v64
	v_add_f32_e32 v64, v223, v64
	v_add_f32_e32 v64, v225, v64
	v_add_f32_e32 v64, v222, v64
	v_add_f32_e32 v64, v224, v64
	v_add_f32_e32 v64, v188, v64
	v_exp_f32_e32 v161, v65
	v_add_f32_e32 v64, v191, v64
	v_exp_f32_e32 v162, v66
	v_add_f32_e32 v64, v189, v64
	v_exp_f32_e32 v163, v67
	v_add_f32_e32 v64, v190, v64
	s_waitcnt lgkmcnt(0)
	v_mfma_f32_32x32x16_bf16 v[80:95], v[164:167], v[112:115], v[80:95]
	v_exp_f32_e32 v164, v68
	v_add_f32_e32 v64, v160, v64
	v_exp_f32_e32 v165, v69
	v_add_f32_e32 v64, v161, v64
	v_exp_f32_e32 v166, v70
	v_add_f32_e32 v64, v162, v64
	v_exp_f32_e32 v167, v71
	v_add_f32_e32 v64, v163, v64
	v_add_f32_e32 v64, v164, v64
	v_add_f32_e32 v64, v165, v64
	v_add_f32_e32 v64, v166, v64
	v_add_f32_e32 v64, v167, v64
	v_add_f32_e32 v64, v168, v64
	v_add_f32_e32 v64, v169, v64
	v_add_f32_e32 v64, v170, v64
	v_add_f32_e32 v64, v171, v64
	v_add_f32_e32 v64, v172, v64
	v_add_f32_e32 v64, v173, v64
	v_add_f32_e32 v64, v174, v64
	v_add_f32_e32 v234, v79, v64
	v_cvt_pk_bf16_f32 v64, v231, v233
	v_cvt_pk_bf16_f32 v65, v229, v232
	v_cvt_pk_bf16_f32 v66, v228, v230
	v_cvt_pk_bf16_f32 v67, v226, v227
	v_cvt_pk_bf16_f32 v68, v223, v225
	v_cvt_pk_bf16_f32 v69, v222, v224
	v_cvt_pk_bf16_f32 v70, v188, v191
	v_cvt_pk_bf16_f32 v71, v189, v190
	v_cvt_pk_bf16_f32 v72, v160, v161
	v_cvt_pk_bf16_f32 v73, v162, v163
	v_cvt_pk_bf16_f32 v74, v164, v165
	v_cvt_pk_bf16_f32 v75, v166, v167
	v_cvt_pk_bf16_f32 v76, v168, v169
	v_cvt_pk_bf16_f32 v77, v170, v171
	v_cvt_pk_bf16_f32 v78, v172, v173
	v_cvt_pk_bf16_f32 v79, v174, v79
	s_nop 1
	v_permlane32_swap_b32_e32 v64, v66
	v_permlane32_swap_b32_e32 v65, v67
	v_permlane32_swap_b32_e32 v68, v70
	v_permlane32_swap_b32_e32 v69, v71
	v_permlane32_swap_b32_e32 v72, v74
	v_permlane32_swap_b32_e32 v73, v75
	v_permlane32_swap_b32_e32 v76, v78
	v_permlane32_swap_b32_e32 v77, v79
	v_lshl_add_u64 v[196:197], v[196:197], 0, s[100:101]
	v_lshl_add_u64 v[198:199], v[198:199], 0, s[100:101]
	global_load_dwordx4 v[160:163], v[196:197], off offset:2560
	global_load_dwordx4 v[164:167], v[196:197], off offset:2048
	global_load_dwordx4 v[172:175], v[198:199], off offset:2560
	global_load_dwordx4 v[168:171], v[198:199], off offset:2048
	ds_read_b64_tr_b16 v[222:223], v185 offset:0
	ds_read_b64_tr_b16 v[224:225], v185 offset:0x800
	ds_read_b64_tr_b16 v[226:227], v185 offset:0x1000
	ds_read_b64_tr_b16 v[228:229], v185 offset:0x1800
	ds_read_b64_tr_b16 v[230:231], v185 offset:0x2000
	ds_read_b64_tr_b16 v[232:233], v185 offset:0x2800
	ds_read_b64_tr_b16 v[236:237], v185 offset:0x3000
	ds_read_b64_tr_b16 v[238:239], v185 offset:0x3800
	s_waitcnt lgkmcnt(6)
	s_nop 0
	v_mfma_f32_32x32x16_bf16 v[0:15], v[64:67], v[222:225], v[0:15]
	ds_read_b64_tr_b16 v[222:223], v185 offset:0x200
	ds_read_b64_tr_b16 v[224:225], v185 offset:0xa00
	s_waitcnt lgkmcnt(6)
	v_mfma_f32_32x32x16_bf16 v[0:15], v[68:71], v[226:229], v[0:15]
	ds_read_b64_tr_b16 v[226:227], v185 offset:0x1200
	ds_read_b64_tr_b16 v[228:229], v185 offset:0x1a00
	s_waitcnt lgkmcnt(6)
	v_mfma_f32_32x32x16_bf16 v[0:15], v[72:75], v[230:233], v[0:15]
	ds_read_b64_tr_b16 v[230:231], v185 offset:0x2200
	ds_read_b64_tr_b16 v[232:233], v185 offset:0x2a00
	s_waitcnt lgkmcnt(6)
	v_mfma_f32_32x32x16_bf16 v[0:15], v[76:79], v[236:239], v[0:15]
	ds_read_b64_tr_b16 v[236:237], v185 offset:0x3200
	ds_read_b64_tr_b16 v[238:239], v185 offset:0x3a00
	s_waitcnt lgkmcnt(6)
	v_mfma_f32_32x32x16_bf16 v[16:31], v[64:67], v[222:225], v[16:31]
	ds_read_b64_tr_b16 v[222:223], v185 offset:0x400
	ds_read_b64_tr_b16 v[224:225], v185 offset:0xc00
	s_waitcnt lgkmcnt(6)
	v_mfma_f32_32x32x16_bf16 v[16:31], v[68:71], v[226:229], v[16:31]
	ds_read_b64_tr_b16 v[226:227], v185 offset:0x1400
	ds_read_b64_tr_b16 v[228:229], v185 offset:0x1c00
	s_waitcnt lgkmcnt(6)
	v_mfma_f32_32x32x16_bf16 v[16:31], v[72:75], v[230:233], v[16:31]
	ds_read_b64_tr_b16 v[230:231], v185 offset:0x2400
	ds_read_b64_tr_b16 v[232:233], v185 offset:0x2c00
	s_waitcnt lgkmcnt(6)
	v_mfma_f32_32x32x16_bf16 v[16:31], v[76:79], v[236:239], v[16:31]
	ds_read_b64_tr_b16 v[236:237], v185 offset:0x3400
	ds_read_b64_tr_b16 v[238:239], v185 offset:0x3c00
	s_waitcnt lgkmcnt(6)
	v_mfma_f32_32x32x16_bf16 v[32:47], v[64:67], v[222:225], v[32:47]
	ds_read_b64_tr_b16 v[222:223], v185 offset:0x600
	ds_read_b64_tr_b16 v[224:225], v185 offset:0xe00
	s_waitcnt vmcnt(4)
	ds_write_b128 v206, v[148:151] offset:32768
	ds_write_b128 v207, v[156:159] offset:32768
	s_waitcnt lgkmcnt(8)
	v_mfma_f32_32x32x16_bf16 v[32:47], v[68:71], v[226:229], v[32:47]
	ds_read_b64_tr_b16 v[226:227], v185 offset:0x1600
	ds_read_b64_tr_b16 v[228:229], v185 offset:0x1e00
	s_waitcnt lgkmcnt(8)
	v_mfma_f32_32x32x16_bf16 v[32:47], v[72:75], v[230:233], v[32:47]
	ds_read_b64_tr_b16 v[230:231], v185 offset:0x2600
	ds_read_b64_tr_b16 v[232:233], v185 offset:0x2e00
	s_waitcnt lgkmcnt(8)
	v_mfma_f32_32x32x16_bf16 v[32:47], v[76:79], v[236:239], v[32:47]
	ds_read_b64_tr_b16 v[236:237], v185 offset:0x3600
	ds_read_b64_tr_b16 v[238:239], v185 offset:0x3e00
	s_waitcnt lgkmcnt(8)
	v_mfma_f32_32x32x16_bf16 v[48:63], v[64:67], v[222:225], v[48:63]
	s_waitcnt lgkmcnt(0)
	s_barrier
	s_waitcnt vmcnt(4)
	v_exp_f32_e32 v218, v96
	v_exp_f32_e32 v219, v97
	v_exp_f32_e32 v220, v98
	v_mfma_f32_32x32x16_bf16 v[48:63], v[68:71], v[226:229], v[48:63]
	v_exp_f32_e32 v221, v99
	v_exp_f32_e32 v240, v108
	v_exp_f32_e32 v241, v109
	v_exp_f32_e32 v242, v110
	v_exp_f32_e32 v243, v111
	s_waitcnt vmcnt(7)
	ds_write_b128 v204, v[144:147]
	s_waitcnt vmcnt(6)
	ds_write_b128 v205, v[152:155]
	v_mfma_f32_32x32x16_bf16 v[48:63], v[72:75], v[230:233], v[48:63]
	v_exp_f32_e32 v230, v100
	v_exp_f32_e32 v231, v101
	v_exp_f32_e32 v232, v102
	v_exp_f32_e32 v233, v103
	v_mfma_f32_32x32x16_bf16 v[48:63], v[76:79], v[236:239], v[48:63]
	v_exp_f32_e32 v236, v104
	v_exp_f32_e32 v237, v105
	v_exp_f32_e32 v238, v106
	v_exp_f32_e32 v239, v107
	ds_read_b128 v[64:67], v212 offset:32768
	ds_read_b128 v[68:71], v212 offset:40960
	ds_read_b128 v[222:225], v211 offset:32768
	ds_read_b128 v[226:229], v211 offset:40960
	v_exp_f32_e32 v244, v86
	v_exp_f32_e32 v245, v87
	s_waitcnt lgkmcnt(3)
	v_mfma_f32_32x32x16_bf16 v[96:111], v[64:67], v[140:143], 0
	v_exp_f32_e32 v246, v88
	v_exp_f32_e32 v247, v89
	v_exp_f32_e32 v248, v90
	v_exp_f32_e32 v249, v91
	v_exp_f32_e32 v250, v92
	v_exp_f32_e32 v251, v93
	v_exp_f32_e32 v252, v94
	s_waitcnt lgkmcnt(2)
	v_mfma_f32_32x32x16_bf16 v[64:79], v[68:71], v[140:143], 0
	v_exp_f32_e32 v95, v95
	s_waitcnt lgkmcnt(1)
	v_mfma_f32_32x32x16_bf16 v[96:111], v[222:225], v[136:139], v[96:111]
	s_waitcnt lgkmcnt(0)
	v_mfma_f32_32x32x16_bf16 v[64:79], v[226:229], v[136:139], v[64:79]
	ds_read_b128 v[222:225], v210 offset:32768
	ds_read_b128 v[226:229], v210 offset:40960
	s_waitcnt lgkmcnt(1)
	v_mfma_f32_32x32x16_bf16 v[96:111], v[222:225], v[132:135], v[96:111]
	s_waitcnt lgkmcnt(0)
	v_mfma_f32_32x32x16_bf16 v[64:79], v[226:229], v[132:135], v[64:79]
	ds_read_b128 v[222:225], v209 offset:32768
	ds_read_b128 v[226:229], v209 offset:40960
	s_waitcnt lgkmcnt(1)
	v_mfma_f32_32x32x16_bf16 v[96:111], v[222:225], v[128:131], v[96:111]
	s_waitcnt lgkmcnt(0)
	v_mfma_f32_32x32x16_bf16 v[64:79], v[226:229], v[128:131], v[64:79]
	ds_read_b128 v[222:225], v208 offset:32768
	ds_read_b128 v[226:229], v208 offset:40960
	s_waitcnt lgkmcnt(1)
	v_mfma_f32_32x32x16_bf16 v[96:111], v[222:225], v[124:127], v[96:111]
	s_waitcnt lgkmcnt(0)
	v_mfma_f32_32x32x16_bf16 v[64:79], v[226:229], v[124:127], v[64:79]
	ds_read_b128 v[222:225], v213 offset:32768
	ds_read_b128 v[226:229], v213 offset:40960
	s_waitcnt lgkmcnt(1)
	v_mfma_f32_32x32x16_bf16 v[96:111], v[222:225], v[120:123], v[96:111]
	s_waitcnt lgkmcnt(0)
	v_mfma_f32_32x32x16_bf16 v[64:79], v[226:229], v[120:123], v[64:79]
	ds_read_b128 v[222:225], v214 offset:32768
	ds_read_b128 v[226:229], v214 offset:40960
	s_waitcnt lgkmcnt(1)
	v_mfma_f32_32x32x16_bf16 v[96:111], v[222:225], v[116:119], v[96:111]
	s_waitcnt lgkmcnt(0)
	v_mfma_f32_32x32x16_bf16 v[64:79], v[226:229], v[116:119], v[64:79]
	ds_read_b128 v[222:225], v215 offset:32768
	ds_read_b128 v[226:229], v215 offset:40960
	s_waitcnt lgkmcnt(1)
	v_mfma_f32_32x32x16_bf16 v[96:111], v[222:225], v[112:115], v[96:111]
	v_exp_f32_e32 v224, v80
	v_add_f32_e32 v80, v219, v218
	v_add_f32_e32 v80, v220, v80
	v_add_f32_e32 v80, v221, v80
	v_add_f32_e32 v80, v230, v80
	v_add_f32_e32 v80, v231, v80
	v_add_f32_e32 v80, v232, v80
	v_add_f32_e32 v80, v233, v80
	v_add_f32_e32 v80, v236, v80
	v_add_f32_e32 v80, v237, v80
	v_add_f32_e32 v80, v238, v80
	v_add_f32_e32 v80, v239, v80
	v_add_f32_e32 v80, v240, v80
	v_exp_f32_e32 v225, v81
	v_add_f32_e32 v80, v241, v80
	s_waitcnt lgkmcnt(0)
	v_mfma_f32_32x32x16_bf16 v[64:79], v[226:229], v[112:115], v[64:79]
	v_exp_f32_e32 v226, v82
	v_add_f32_e32 v80, v242, v80
	v_exp_f32_e32 v227, v83
	v_add_f32_e32 v80, v243, v80
	v_exp_f32_e32 v228, v84
	v_add_f32_e32 v80, v224, v80
	v_exp_f32_e32 v229, v85
	v_add_f32_e32 v80, v225, v80
	v_add_f32_e32 v80, v226, v80
	v_add_f32_e32 v80, v227, v80
	v_add_f32_e32 v80, v228, v80
	v_add_f32_e32 v80, v229, v80
	v_add_f32_e32 v80, v244, v80
	v_add_f32_e32 v80, v245, v80
	v_add_f32_e32 v80, v246, v80
	v_add_f32_e32 v80, v247, v80
	v_add_f32_e32 v80, v248, v80
	v_add_f32_e32 v80, v249, v80
	v_add_f32_e32 v80, v250, v80
	v_add_f32_e32 v80, v251, v80
	v_add_f32_e32 v80, v252, v80
	v_add_f32_e32 v222, v95, v80
	v_cvt_pk_bf16_f32 v80, v218, v219
	v_cvt_pk_bf16_f32 v81, v220, v221
	v_cvt_pk_bf16_f32 v82, v230, v231
	v_cvt_pk_bf16_f32 v83, v232, v233
	v_cvt_pk_bf16_f32 v84, v236, v237
	v_cvt_pk_bf16_f32 v85, v238, v239
	v_cvt_pk_bf16_f32 v86, v240, v241
	v_cvt_pk_bf16_f32 v87, v242, v243
	v_cvt_pk_bf16_f32 v88, v224, v225
	v_cvt_pk_bf16_f32 v89, v226, v227
	v_cvt_pk_bf16_f32 v90, v228, v229
	v_cvt_pk_bf16_f32 v91, v244, v245
	v_cvt_pk_bf16_f32 v92, v246, v247
	v_cvt_pk_bf16_f32 v93, v248, v249
	v_cvt_pk_bf16_f32 v94, v250, v251
	v_cvt_pk_bf16_f32 v95, v252, v95
	s_nop 1
	v_permlane32_swap_b32_e32 v80, v82
	v_permlane32_swap_b32_e32 v81, v83
	v_permlane32_swap_b32_e32 v84, v86
	v_permlane32_swap_b32_e32 v85, v87
	v_permlane32_swap_b32_e32 v88, v90
	v_permlane32_swap_b32_e32 v89, v91
	v_permlane32_swap_b32_e32 v92, v94
	v_permlane32_swap_b32_e32 v93, v95
	s_cmpk_gt_u32 s8, 0x100
	s_cselect_b64 s[6:7], -1, 0
	v_lshl_add_u64 v[196:197], v[196:197], 0, s[100:101]
	v_lshl_add_u64 v[198:199], v[198:199], 0, s[100:101]
	global_load_dwordx4 v[144:147], v[196:197], off offset:2560
	global_load_dwordx4 v[148:151], v[196:197], off offset:2048
	global_load_dwordx4 v[152:155], v[198:199], off offset:2560
	global_load_dwordx4 v[156:159], v[198:199], off offset:2048
	s_branch .LBB0_592
.Lga_exit:
	v_mov_b32_e32 v235, v183
	s_nop 1
	v_permlane32_swap_b32_e32 v183, v235
	v_add_f32_e32 v183, v183, v235
	s_waitcnt lgkmcnt(0)
	s_barrier

.LBB0_597:
	v_mov_b64_e32 v[196:197], 0x200
	v_mov_b64_e32 v[198:199], 0x1ff
	s_cmpk_eq_i32 s14, 0x100
	s_cselect_b64 s[0:1], -1, 0
	s_and_b64 s[2:3], s[0:1], exec
	v_readlane_b32 s2, v254, 0
	v_readlane_b32 s3, v254, 13
	s_cselect_b32 s22, s3, s2
	s_cmp_lt_i32 s22, 0
	s_cbranch_scc1 .LBB0_691
	v_writelane_b32 v254, s27, 45
	s_and_b64 s[0:1], s[0:1], exec
	v_writelane_b32 v254, s26, 46
	s_cselect_b32 s0, 0x80, s14
	v_writelane_b32 v254, s0, 47
	s_cmpk_gt_u32 s22, 0x17f
	v_writelane_b32 v254, s22, 48
	s_cbranch_scc1 .LBB0_631
	v_readlane_b32 s0, v254, 35
	s_mulk_i32 s0, 0x2b98
	v_readlane_b32 s1, v254, 36
	s_add_u32 s0, s12, s0
	s_addc_u32 s1, s13, 0
	v_writelane_b32 v254, s0, 49
	s_nop 1
	v_writelane_b32 v254, s1, 50
	s_nop 0
	v_readlane_b32 s0, v254, 39
	s_add_u32 s1, s0, 0x11800600
	v_writelane_b32 v254, s1, 51
	s_nop 0
	v_readlane_b32 s1, v254, 40
	s_addc_u32 s2, s1, 0
	v_writelane_b32 v254, s2, 52
	s_add_u32 s0, s0, 0x11800c00
	v_writelane_b32 v254, s0, 53
	s_addc_u32 s0, s1, 0
	v_writelane_b32 v254, s0, 54
	v_writelane_b32 v254, s34, 55
	s_mov_b32 s1, s22
	v_writelane_b32 v254, s35, 56
	s_branch .LBB0_601

	.amdhsa_kernel _Z6mk_fwd5FArgs
		.amdhsa_group_segment_fixed_size 0
		.amdhsa_private_segment_fixed_size 0
		.amdhsa_kernarg_size 448
		.amdhsa_user_sgpr_count 2
		.amdhsa_user_sgpr_dispatch_ptr 0
		.amdhsa_user_sgpr_queue_ptr 0
		.amdhsa_user_sgpr_kernarg_segment_ptr 1
		.amdhsa_user_sgpr_dispatch_id 0
		.amdhsa_user_sgpr_kernarg_preload_length 0
		.amdhsa_user_sgpr_kernarg_preload_offset 0
		.amdhsa_user_sgpr_private_segment_size 0
		.amdhsa_uses_dynamic_stack 0
		.amdhsa_enable_private_segment 0
		.amdhsa_system_sgpr_workgroup_id_x 1
		.amdhsa_system_sgpr_workgroup_id_y 0
		.amdhsa_system_sgpr_workgroup_id_z 0
		.amdhsa_system_sgpr_workgroup_info 0
		.amdhsa_system_vgpr_workitem_id 0
		.amdhsa_next_free_vgpr 256
		.amdhsa_next_free_sgpr 102
		.amdhsa_accum_offset 256
		.amdhsa_reserve_vcc 1
		.amdhsa_float_round_mode_32 0
		.amdhsa_float_round_mode_16_64 0
		.amdhsa_float_denorm_mode_32 3
		.amdhsa_float_denorm_mode_16_64 3
		.amdhsa_dx10_clamp 1
		.amdhsa_ieee_mode 1
		.amdhsa_fp16_overflow 0
		.amdhsa_tg_split 0
		.amdhsa_exception_fp_ieee_invalid_op 0
		.amdhsa_exception_fp_denorm_src 0
		.amdhsa_exception_fp_ieee_div_zero 0
		.amdhsa_exception_fp_ieee_overflow 0
		.amdhsa_exception_fp_ieee_underflow 0
		.amdhsa_exception_fp_ieee_inexact 0
		.amdhsa_exception_int_div_zero 0
	.end_amdhsa_kernel

amdhsa.kernels:
  - .agpr_count:     0
    .args:
      - .offset:         0
        .size:           192
        .value_kind:     by_value
      - .offset:         192
        .size:           4
        .value_kind:     hidden_block_count_x
      - .offset:         196
        .size:           4
        .value_kind:     hidden_block_count_y
      - .offset:         200
        .size:           4
        .value_kind:     hidden_block_count_z
      - .offset:         204
        .size:           2
        .value_kind:     hidden_group_size_x
      - .offset:         206
        .size:           2
        .value_kind:     hidden_group_size_y
      - .offset:         208
        .size:           2
        .value_kind:     hidden_group_size_z
      - .offset:         210
        .size:           2
        .value_kind:     hidden_remainder_x
      - .offset:         212
        .size:           2
        .value_kind:     hidden_remainder_y
      - .offset:         214
        .size:           2
        .value_kind:     hidden_remainder_z
      - .offset:         232
        .size:           8
        .value_kind:     hidden_global_offset_x
      - .offset:         240
        .size:           8
        .value_kind:     hidden_global_offset_y
      - .offset:         248
        .size:           8
        .value_kind:     hidden_global_offset_z
      - .offset:         256
        .size:           2
        .value_kind:     hidden_grid_dims
      - .offset:         312
        .size:           4
        .value_kind:     hidden_dynamic_lds_size
    .group_segment_fixed_size: 0
    .kernarg_segment_align: 8
    .kernarg_segment_size: 448
    .language:       OpenCL C
    .language_version:
      - 2
      - 0
    .max_flat_workgroup_size: 512
    .name:           _Z6mk_fwd5FArgs
    .private_segment_fixed_size: 0
    .sgpr_count:     108
    .sgpr_spill_count: 132
    .symbol:         _Z6mk_fwd5FArgs.kd
    .uniform_work_group_size: 1
    .uses_dynamic_stack: false
    .vgpr_count:     256
    .vgpr_spill_count: 0
    .wavefront_size: 64
